# baseline (speedup 1.0000x reference)
.LBB1_8:
	s_or_b64 exec, exec, s[4:5]
	v_add_u32_e32 v10, v172, v2
	s_waitcnt vmcnt(1) lgkmcnt(0)
	s_barrier
	ds_read_b128 v[18:21], v10 offset:256
	ds_read_b128 v[22:25], v10 offset:288
	ds_read_b128 v[82:85], v10 offset:320
	ds_read_b128 v[86:89], v10 offset:352
	ds_read_b128 v[74:77], v10 offset:384
	ds_read_b128 v[78:81], v10 offset:416
	ds_read_b128 v[2:5], v213 offset:32768
	ds_read_b128 v[6:9], v213 offset:0
	ds_read_b128 v[66:69], v10 offset:448
	ds_read_b128 v[70:73], v10 offset:480
	ds_read_b128 v[10:13], v213 offset:1024
	s_waitcnt lgkmcnt(3)
	v_pk_mul_f32 v[26:27], v[8:9], v[20:21]
	v_pk_mul_f32 v[28:29], v[6:7], v[18:19]
	ds_read_b128 v[14:17], v213 offset:8192
	s_waitcnt lgkmcnt(1)
	v_pk_mul_f32 v[12:13], v[12:13], v[24:25]
	v_pk_mul_f32 v[10:11], v[10:11], v[22:23]
	v_pk_fma_f32 v[30:31], v[8:9], v[20:21], v[12:13]
	v_pk_fma_f32 v[32:33], v[6:7], v[18:19], v[10:11]
	v_cvt_pk_bf16_f32 v9, v12, v13
	v_cvt_pk_bf16_f32 v7, v26, v27
	v_cvt_pk_bf16_f32 v8, v10, v11
	v_cvt_pk_bf16_f32 v6, v28, v29
	ds_read_b128 v[10:13], v213 offset:33792
	s_nop 0
	v_mfma_f32_32x32x16_bf16 v[34:49], v[2:5], v[6:9], 0
	ds_read_b128 v[6:9], v213 offset:9216
	s_waitcnt lgkmcnt(2)
	v_mul_f32_e32 v26, v16, v20
	v_mul_f32_e32 v27, v17, v21
	v_pk_mul_f32 v[50:51], v[14:15], v[18:19]
	s_mov_b32 s4, 0x3727c5ac
	s_waitcnt lgkmcnt(0)
	v_pk_mul_f32 v[8:9], v[8:9], v[24:25]
	v_pk_mul_f32 v[28:29], v[6:7], v[22:23]
	v_pk_fma_f32 v[90:91], v[16:17], v[20:21], v[8:9]
	v_pk_fma_f32 v[92:93], v[14:15], v[18:19], v[28:29]
	ds_read_b128 v[14:17], v213 offset:2048
	v_cvt_pk_bf16_f32 v9, v8, v9
	v_cvt_pk_bf16_f32 v7, v26, v27
	v_cvt_pk_bf16_f32 v8, v28, v29
	ds_read_b128 v[26:29], v213 offset:3072
	v_cvt_pk_bf16_f32 v6, v50, v51
	s_waitcnt lgkmcnt(1)
	v_pk_mul_f32 v[94:95], v[14:15], v[82:83]
	s_mov_b32 s0, 0x3c800000
	v_mfma_f32_32x32x16_bf16 v[50:65], v[2:5], v[6:9], 0
	v_mul_f32_e32 v2, v16, v84
	v_mul_f32_e32 v3, v17, v85
	s_waitcnt lgkmcnt(0)
	v_mul_f32_e32 v4, v28, v88
	v_mul_f32_e32 v5, v29, v89
	v_pk_mul_f32 v[6:7], v[26:27], v[86:87]
	v_pk_fma_f32 v[8:9], v[16:17], v[84:85], v[4:5]
	v_cvt_pk_bf16_f32 v3, v2, v3
	v_pk_fma_f32 v[14:15], v[14:15], v[82:83], v[6:7]
	v_pk_add_f32 v[26:27], v[8:9], v[30:31]
	v_cvt_pk_bf16_f32 v5, v4, v5
	v_cvt_pk_bf16_f32 v4, v6, v7
	ds_read_b128 v[6:9], v213 offset:10240
	v_pk_add_f32 v[28:29], v[14:15], v[32:33]
	ds_read_b128 v[14:17], v213 offset:11264
	v_cvt_pk_bf16_f32 v2, v94, v95
	s_waitcnt lgkmcnt(1)
	v_pk_mul_f32 v[30:31], v[6:7], v[82:83]
	v_mov_b64_e32 v[152:153], s[4:5]
	v_mfma_f32_32x32x16_bf16 v[34:49], v[10:13], v[2:5], v[34:49]
	v_mul_f32_e32 v2, v8, v84
	v_mul_f32_e32 v3, v9, v85
	s_waitcnt lgkmcnt(0)
	v_mul_f32_e32 v4, v16, v88
	v_mul_f32_e32 v5, v17, v89
	v_pk_mul_f32 v[14:15], v[14:15], v[86:87]
	v_pk_fma_f32 v[8:9], v[8:9], v[84:85], v[4:5]
	v_pk_fma_f32 v[6:7], v[6:7], v[82:83], v[14:15]
	v_cvt_pk_bf16_f32 v5, v4, v5
	v_cvt_pk_bf16_f32 v3, v2, v3
	v_cvt_pk_bf16_f32 v4, v14, v15
	v_pk_add_f32 v[32:33], v[8:9], v[90:91]
	v_pk_add_f32 v[90:91], v[6:7], v[92:93]
	ds_read_b128 v[6:9], v213 offset:34816
	ds_read_b128 v[14:17], v213 offset:4096
	v_cvt_pk_bf16_f32 v2, v30, v31
	s_mov_b32 s13, 0
	s_mov_b64 s[6:7], 0
	v_mfma_f32_32x32x16_bf16 v[50:65], v[10:13], v[2:5], v[50:65]
	ds_read_b128 v[2:5], v213 offset:5120
	ds_read_b128 v[10:13], v213 offset:12288
	s_waitcnt lgkmcnt(2)
	v_pk_mul_f32 v[30:31], v[16:17], v[76:77]
	v_pk_mul_f32 v[92:93], v[14:15], v[74:75]
	s_waitcnt lgkmcnt(1)
	v_pk_mul_f32 v[4:5], v[4:5], v[80:81]
	v_pk_mul_f32 v[94:95], v[2:3], v[78:79]
	v_pk_fma_f32 v[2:3], v[16:17], v[76:77], v[4:5]
	v_cvt_pk_bf16_f32 v5, v4, v5
	v_pk_add_f32 v[96:97], v[2:3], v[26:27]
	v_cvt_pk_bf16_f32 v3, v30, v31
	v_cvt_pk_bf16_f32 v4, v94, v95
	v_cvt_pk_bf16_f32 v2, v92, v93
	v_pk_fma_f32 v[14:15], v[14:15], v[74:75], v[94:95]
	s_waitcnt lgkmcnt(0)
	v_pk_mul_f32 v[30:31], v[10:11], v[74:75]
	v_mfma_f32_32x32x16_bf16 v[34:49], v[6:9], v[2:5], v[34:49]
	ds_read_b128 v[2:5], v213 offset:13312
	v_add_f32_e32 v98, v14, v28
	v_add_f32_e32 v99, v15, v29
	ds_read_b128 v[14:17], v213 offset:35840
	v_pk_mul_f32 v[26:27], v[12:13], v[76:77]
	s_waitcnt lgkmcnt(1)
	v_pk_mul_f32 v[4:5], v[4:5], v[80:81]
	v_pk_mul_f32 v[28:29], v[2:3], v[78:79]
	v_pk_fma_f32 v[2:3], v[12:13], v[76:77], v[4:5]
	v_pk_fma_f32 v[10:11], v[10:11], v[74:75], v[28:29]
	v_pk_add_f32 v[32:33], v[2:3], v[32:33]
	v_pk_add_f32 v[92:93], v[10:11], v[90:91]
	ds_read_b128 v[10:13], v213 offset:6144
	v_cvt_pk_bf16_f32 v5, v4, v5
	v_cvt_pk_bf16_f32 v3, v26, v27
	v_cvt_pk_bf16_f32 v4, v28, v29
	ds_read_b128 v[26:29], v213 offset:7168
	v_cvt_pk_bf16_f32 v2, v30, v31
	s_waitcnt lgkmcnt(1)
	v_pk_mul_f32 v[30:31], v[10:11], v[66:67]
	v_mfma_f32_32x32x16_bf16 v[50:65], v[6:9], v[2:5], v[50:65]
	v_mul_f32_e32 v2, v12, v68
	v_mul_f32_e32 v3, v13, v69
	s_waitcnt lgkmcnt(0)
	v_mul_f32_e32 v4, v28, v72
	v_mul_f32_e32 v5, v29, v73
	v_pk_mul_f32 v[6:7], v[26:27], v[70:71]
	v_pk_fma_f32 v[8:9], v[12:13], v[68:69], v[4:5]
	v_cvt_pk_bf16_f32 v3, v2, v3
	v_pk_fma_f32 v[10:11], v[10:11], v[66:67], v[6:7]
	v_pk_add_f32 v[94:95], v[8:9], v[96:97]
	v_cvt_pk_bf16_f32 v5, v4, v5
	v_cvt_pk_bf16_f32 v4, v6, v7
	ds_read_b128 v[6:9], v213 offset:14336
	v_pk_add_f32 v[96:97], v[10:11], v[98:99]
	ds_read_b128 v[10:13], v213 offset:15360
	v_cvt_pk_bf16_f32 v2, v30, v31
	s_waitcnt lgkmcnt(1)
	v_pk_mul_f32 v[30:31], v[6:7], v[66:67]
	v_mfma_f32_32x32x16_bf16 v[34:49], v[14:17], v[2:5], v[34:49]
	s_waitcnt lgkmcnt(0)
	v_mul_f32_e32 v10, v10, v70
	v_mul_f32_e32 v11, v11, v71
	v_mul_f32_e32 v2, v8, v68
	v_mul_f32_e32 v3, v9, v69
	v_pk_mul_f32 v[4:5], v[12:13], v[72:73]
	v_pk_fma_f32 v[6:7], v[6:7], v[66:67], v[10:11]
	v_pk_fma_f32 v[8:9], v[8:9], v[68:69], v[4:5]
	v_pk_add_f32 v[92:93], v[6:7], v[92:93]
	v_cvt_pk_bf16_f32 v3, v2, v3
	v_pk_add_f32 v[90:91], v[8:9], v[32:33]
	v_cvt_pk_bf16_f32 v5, v4, v5
	v_cvt_pk_bf16_f32 v4, v10, v11
	ds_read_b128 v[26:29], v213 offset:36864
	ds_read_b128 v[6:9], v213 offset:16384
	v_cvt_pk_bf16_f32 v2, v30, v31
	ds_read_b128 v[98:101], v213 offset:25600
	ds_read_b128 v[102:105], v213 offset:37888
	v_mfma_f32_32x32x16_bf16 v[50:65], v[14:17], v[2:5], v[50:65]
	ds_read_b128 v[2:5], v213 offset:17408
	ds_read_b128 v[30:33], v213 offset:24576
	s_waitcnt lgkmcnt(4)
	v_pk_mul_f32 v[12:13], v[6:7], v[18:19]
	v_pk_mul_f32 v[10:11], v[8:9], v[20:21]
	s_waitcnt lgkmcnt(1)
	v_pk_mul_f32 v[14:15], v[2:3], v[22:23]
	v_pk_mul_f32 v[22:23], v[98:99], v[22:23]
	v_pk_fma_f32 v[112:113], v[6:7], v[18:19], v[14:15]
	s_waitcnt lgkmcnt(0)
	v_pk_mul_f32 v[114:115], v[30:31], v[18:19]
	v_pk_fma_f32 v[118:119], v[30:31], v[18:19], v[22:23]
	v_pk_mul_f32 v[4:5], v[4:5], v[24:25]
	v_pk_mul_f32 v[106:107], v[32:33], v[20:21]
	v_pk_mul_f32 v[24:25], v[100:101], v[24:25]
	ds_read_b128 v[98:101], v213 offset:18432
	v_cvt_pk_bf16_f32 v19, v106, v107
	ds_read_b128 v[106:109], v213 offset:19456
	v_pk_fma_f32 v[110:111], v[8:9], v[20:21], v[4:5]
	v_cvt_pk_bf16_f32 v5, v4, v5
	v_cvt_pk_bf16_f32 v3, v10, v11
	v_cvt_pk_bf16_f32 v4, v14, v15
	s_waitcnt lgkmcnt(0)
	v_pk_mul_f32 v[106:107], v[106:107], v[86:87]
	v_cvt_pk_bf16_f32 v2, v12, v13
	v_pk_mul_f32 v[120:121], v[98:99], v[82:83]
	v_pk_mul_f32 v[108:109], v[108:109], v[88:89]
	v_pk_fma_f32 v[98:99], v[98:99], v[82:83], v[106:107]
	v_mfma_f32_32x32x16_bf16 v[2:17], v[26:29], v[2:5], 0
	v_cvt_pk_bf16_f32 v18, v114, v115
	v_mul_f32_e32 v114, v100, v84
	v_mul_f32_e32 v115, v101, v85
	v_fma_f32 v100, v100, v84, v108
	v_fma_f32 v101, v101, v85, v109
	v_pk_add_f32 v[124:125], v[98:99], v[112:113]
	v_pk_add_f32 v[122:123], v[100:101], v[110:111]
	v_cvt_pk_bf16_f32 v101, v108, v109
	v_cvt_pk_bf16_f32 v100, v106, v107
	ds_read_b128 v[106:109], v213 offset:26624
	v_pk_fma_f32 v[116:117], v[32:33], v[20:21], v[24:25]
	v_cvt_pk_bf16_f32 v21, v24, v25
	v_cvt_pk_bf16_f32 v20, v22, v23
	ds_read_b128 v[110:113], v213 offset:27648
	v_cvt_pk_bf16_f32 v99, v114, v115
	v_mfma_f32_32x32x16_bf16 v[18:33], v[26:29], v[18:21], 0
	v_cvt_pk_bf16_f32 v98, v120, v121
	s_waitcnt lgkmcnt(1)
	v_mul_f32_e32 v114, v106, v82
	v_mul_f32_e32 v115, v107, v83
	s_waitcnt lgkmcnt(0)
	v_pk_mul_f32 v[86:87], v[110:111], v[86:87]
	v_pk_mul_f32 v[88:89], v[112:113], v[88:89]
	v_pk_fma_f32 v[82:83], v[106:107], v[82:83], v[86:87]
	v_mfma_f32_32x32x16_bf16 v[2:17], v[102:105], v[98:101], v[2:17]
	v_mul_f32_e32 v98, v108, v84
	v_mul_f32_e32 v99, v109, v85
	v_fma_f32 v84, v108, v84, v88
	v_fma_f32 v85, v109, v85, v89
	v_add_f32_e32 v108, v82, v118
	v_add_f32_e32 v109, v83, v119
	v_cvt_pk_bf16_f32 v83, v98, v99
	v_pk_add_f32 v[106:107], v[84:85], v[116:117]
	v_cvt_pk_bf16_f32 v85, v88, v89
	v_cvt_pk_bf16_f32 v84, v86, v87
	ds_read_b128 v[86:89], v213 offset:38912
	ds_read_b128 v[98:101], v213 offset:20480
	v_cvt_pk_bf16_f32 v82, v114, v115
	s_waitcnt lgkmcnt(0)
	v_pk_mul_f32 v[110:111], v[100:101], v[76:77]
	v_mfma_f32_32x32x16_bf16 v[18:33], v[102:105], v[82:85], v[18:33]
	ds_read_b128 v[82:85], v213 offset:21504
	ds_read_b128 v[102:105], v213 offset:28672
	v_mul_f32_e32 v112, v98, v74
	v_mul_f32_e32 v113, v99, v75
	s_waitcnt lgkmcnt(1)
	v_pk_mul_f32 v[84:85], v[84:85], v[80:81]
	v_pk_mul_f32 v[114:115], v[82:83], v[78:79]
	v_pk_fma_f32 v[82:83], v[100:101], v[76:77], v[84:85]
	v_cvt_pk_bf16_f32 v85, v84, v85
	v_pk_add_f32 v[116:117], v[82:83], v[122:123]
	v_cvt_pk_bf16_f32 v83, v110, v111
	v_cvt_pk_bf16_f32 v84, v114, v115
	v_cvt_pk_bf16_f32 v82, v112, v113
	v_pk_fma_f32 v[98:99], v[98:99], v[74:75], v[114:115]
	s_waitcnt lgkmcnt(0)
	v_pk_mul_f32 v[112:113], v[102:103], v[74:75]
	v_mfma_f32_32x32x16_bf16 v[2:17], v[86:89], v[82:85], v[2:17]
	ds_read_b128 v[82:85], v213 offset:29696
	v_add_f32_e32 v118, v98, v124
	v_add_f32_e32 v119, v99, v125
	v_mul_f32_e32 v110, v104, v76
	v_mul_f32_e32 v111, v105, v77
	ds_read_b128 v[98:101], v213 offset:39936
	s_waitcnt lgkmcnt(1)
	v_pk_mul_f32 v[78:79], v[82:83], v[78:79]
	v_pk_mul_f32 v[80:81], v[84:85], v[80:81]
	v_pk_fma_f32 v[74:75], v[102:103], v[74:75], v[78:79]
	v_pk_fma_f32 v[76:77], v[104:105], v[76:77], v[80:81]
	v_pk_add_f32 v[104:105], v[74:75], v[108:109]
	v_pk_add_f32 v[102:103], v[76:77], v[106:107]
	v_cvt_pk_bf16_f32 v77, v80, v81
	v_cvt_pk_bf16_f32 v76, v78, v79
	ds_read_b128 v[78:81], v213 offset:22528
	ds_read_b128 v[82:85], v213 offset:23552
	v_cvt_pk_bf16_f32 v75, v110, v111
	v_cvt_pk_bf16_f32 v74, v112, v113
	s_waitcnt lgkmcnt(0)
	v_pk_mul_f32 v[82:83], v[82:83], v[70:71]
	v_mfma_f32_32x32x16_bf16 v[18:33], v[86:89], v[74:77], v[18:33]
	v_mul_f32_e32 v74, v80, v68
	v_mul_f32_e32 v75, v81, v69
	v_mul_f32_e32 v76, v84, v72
	v_mul_f32_e32 v77, v85, v73
	v_mul_f32_e32 v86, v78, v66
	v_mul_f32_e32 v87, v79, v67
	v_pk_fma_f32 v[80:81], v[80:81], v[68:69], v[76:77]
	v_pk_fma_f32 v[78:79], v[78:79], v[66:67], v[82:83]
	v_cvt_pk_bf16_f32 v75, v74, v75
	v_pk_add_f32 v[88:89], v[80:81], v[116:117]
	v_pk_add_f32 v[106:107], v[78:79], v[118:119]
	ds_read_b128 v[78:81], v213 offset:30720
	v_cvt_pk_bf16_f32 v77, v76, v77
	v_cvt_pk_bf16_f32 v76, v82, v83
	ds_read_b128 v[82:85], v213 offset:31744
	v_cvt_pk_bf16_f32 v74, v86, v87
	s_waitcnt lgkmcnt(0)
	v_pk_mul_f32 v[72:73], v[84:85], v[72:73]
	v_mfma_f32_32x32x16_bf16 v[2:17], v[98:101], v[74:77], v[2:17]
	v_mul_f32_e32 v74, v80, v68
	v_mul_f32_e32 v75, v81, v69
	v_fma_f32 v68, v80, v68, v72
	v_fma_f32 v69, v81, v69, v73
	v_mul_f32_e32 v70, v82, v70
	v_mul_f32_e32 v71, v83, v71
	v_pk_add_f32 v[84:85], v[68:69], v[102:103]
	v_cvt_pk_bf16_f32 v69, v72, v73
	v_pk_mov_b32 v[72:73], v[96:97], v[94:95] op_sel:[1,0]
	v_mov_b32_e32 v97, v95
	v_pk_add_f32 v[72:73], v[72:73], v[96:97]
	v_pk_mul_f32 v[76:77], v[78:79], v[66:67]
	v_pk_fma_f32 v[66:67], v[78:79], v[66:67], v[70:71]
	v_pk_add_f32 v[72:73], v[72:73], v[72:73] op_sel:[0,1] op_sel_hi:[1,0]
	v_pk_add_f32 v[86:87], v[66:67], v[104:105]
	v_mov_b32_e32 v66, v72
	s_nop 1
	v_permlane32_swap_b32_e32 v72, v66
	v_add_f32_e32 v66, v72, v66
	v_cvt_pk_bf16_f32 v67, v74, v75
	v_rcp_f32_e32 v74, v66
	v_cvt_pk_bf16_f32 v68, v70, v71
	v_cvt_pk_bf16_f32 v66, v76, v77
	v_pk_mul_f32 v[70:71], v[46:47], v[74:75] op_sel_hi:[1,0]
	s_nop 0
	v_mfma_f32_32x32x16_bf16 v[18:33], v[98:101], v[66:69], v[18:33]
	v_mul_f32_e32 v66, v42, v74
	v_mul_f32_e32 v67, v43, v74
	v_pk_mov_b32 v[42:43], v[92:93], v[90:91] op_sel:[1,0]
	v_mov_b32_e32 v93, v91
	v_pk_add_f32 v[42:43], v[42:43], v[92:93]
	v_pk_mul_f32 v[68:69], v[44:45], v[74:75] op_sel_hi:[1,0]
	v_pk_add_f32 v[42:43], v[42:43], v[42:43] op_sel:[0,1] op_sel_hi:[1,0]
	v_pk_mov_b32 v[44:45], v[106:107], v[88:89] op_sel:[1,0]
	v_mov_b32_e32 v43, v42
	s_nop 1
	v_permlane32_swap_b32_e32 v42, v43
	v_add_f32_e32 v42, v42, v43
	v_rcp_f32_e32 v42, v42
	v_mov_b32_e32 v107, v89
	v_pk_add_f32 v[44:45], v[44:45], v[106:107]
	v_pk_mul_f32 v[72:73], v[48:49], v[74:75] op_sel_hi:[1,0]
	v_pk_add_f32 v[44:45], v[44:45], v[44:45] op_sel:[0,1] op_sel_hi:[1,0]
	v_pk_mul_f32 v[36:37], v[36:37], v[74:75] op_sel_hi:[1,0]
	v_pk_mul_f32 v[38:39], v[38:39], v[74:75] op_sel_hi:[1,0]
	v_pk_mul_f32 v[40:41], v[40:41], v[74:75] op_sel_hi:[1,0]
	v_pk_mul_f32 v[34:35], v[34:35], v[74:75] op_sel_hi:[1,0]
	v_pk_mul_f32 v[74:75], v[58:59], v[42:43] op_sel_hi:[1,0]
	v_pk_mul_f32 v[78:79], v[60:61], v[42:43] op_sel_hi:[1,0]
	v_pk_mul_f32 v[80:81], v[62:63], v[42:43] op_sel_hi:[1,0]
	v_pk_mul_f32 v[82:83], v[64:65], v[42:43] op_sel_hi:[1,0]
	v_pk_mul_f32 v[92:93], v[52:53], v[42:43] op_sel_hi:[1,0]
	v_mov_b32_e32 v43, v44
	s_nop 1
	v_permlane32_swap_b32_e32 v44, v43
	v_add_f32_e32 v43, v44, v43
	v_rcp_f32_e32 v76, v43
	v_pk_mul_f32 v[96:97], v[54:55], v[42:43] op_sel_hi:[1,0]
	v_pk_mul_f32 v[94:95], v[56:57], v[42:43] op_sel_hi:[1,0]
	v_pk_mul_f32 v[98:99], v[50:51], v[42:43] op_sel_hi:[1,0]
	v_pk_mul_f32 v[100:101], v[4:5], v[76:77] op_sel_hi:[1,0]
	v_pk_mov_b32 v[4:5], v[86:87], v[84:85] op_sel:[1,0]
	v_mov_b32_e32 v87, v85
	v_pk_add_f32 v[4:5], v[4:5], v[86:87]
	v_pk_mul_f32 v[102:103], v[6:7], v[76:77] op_sel_hi:[1,0]
	v_pk_add_f32 v[104:105], v[4:5], v[4:5] op_sel:[0,1] op_sel_hi:[1,0]
	v_cvt_pk_bf16_f32 v7, v40, v41
	s_nop 0
	s_nop 0
	ds_read_b128 v[84:87], v150 offset:52224
	ds_read_b128 v[50:53], v150 offset:35840
	ds_read_b128 v[54:57], v150 offset:36864
	ds_read_b128 v[58:61], v150 offset:37888
	ds_read_b128 v[62:65], v150 offset:38912
	v_cvt_pk_bf16_f32 v6, v38, v39
	v_cvt_pk_bf16_f32 v5, v36, v37
	v_cvt_pk_bf16_f32 v4, v34, v35
	ds_read_b128 v[88:91], v150 offset:53248
	ds_read_b128 v[34:37], v150 offset:39936
	ds_read_b128 v[38:41], v150 offset:40960
	ds_read_b128 v[42:45], v150 offset:41984
	ds_read_b128 v[46:49], v150 offset:43008
	v_cvt_pk_bf16_f32 v95, v94, v95
	v_cvt_pk_bf16_f32 v94, v96, v97
	v_cvt_pk_bf16_f32 v93, v92, v93
	v_cvt_pk_bf16_f32 v92, v98, v99
	s_waitcnt lgkmcnt(5)
	v_mfma_f32_32x32x16_bf16 v[50:65], v[84:87], v[4:7], v[50:65]
	v_mul_f32_e32 v10, v10, v76
	v_mul_f32_e32 v11, v11, v76
	v_mul_f32_e32 v12, v12, v76
	v_mul_f32_e32 v13, v13, v76
	v_mul_f32_e32 v8, v8, v76
	v_mul_f32_e32 v9, v9, v76
	v_mov_b32_e32 v77, v104
	s_nop 1
	v_permlane32_swap_b32_e32 v104, v77
	v_cvt_pk_bf16_f32 v73, v72, v73
	s_waitcnt lgkmcnt(0)
	v_mfma_f32_32x32x16_bf16 v[34:49], v[84:87], v[92:95], v[34:49]
	v_cvt_pk_bf16_f32 v72, v70, v71
	v_cvt_pk_bf16_f32 v70, v66, v67
	v_add_f32_e32 v66, v104, v77
	v_cvt_pk_bf16_f32 v71, v68, v69
	v_rcp_f32_e32 v104, v66
	v_cvt_pk_bf16_f32 v69, v82, v83
	v_cvt_pk_bf16_f32 v68, v80, v81
	v_cvt_pk_bf16_f32 v67, v78, v79
	v_cvt_pk_bf16_f32 v66, v74, v75
	ds_read_b128 v[78:81], v150 offset:54272
	v_mfma_f32_32x32x16_bf16 v[50:65], v[88:91], v[70:73], v[50:65]
	v_mul_f32_e32 v2, v2, v76
	v_mul_f32_e32 v3, v3, v76
	v_mul_f32_e32 v20, v20, v104
	v_mul_f32_e32 v21, v21, v104
	v_cvt_pk_bf16_f32 v85, v8, v9
	v_cvt_pk_bf16_f32 v82, v2, v3
	v_pk_mul_f32 v[2:3], v[22:23], v[104:105] op_sel_hi:[1,0]
	v_pk_mul_f32 v[8:9], v[24:25], v[104:105] op_sel_hi:[1,0]
	v_pk_mul_f32 v[18:19], v[18:19], v[104:105] op_sel_hi:[1,0]
	v_mfma_f32_32x32x16_bf16 v[34:49], v[88:91], v[66:69], v[34:49]
	v_cvt_pk_bf16_f32 v84, v102, v103
	v_cvt_pk_bf16_f32 v83, v100, v101
	ds_read_b128 v[86:89], v150 offset:55296
	v_cvt_pk_bf16_f32 v99, v8, v9
	v_cvt_pk_bf16_f32 v98, v2, v3
	v_cvt_pk_bf16_f32 v97, v20, v21
	v_cvt_pk_bf16_f32 v96, v18, v19
	s_waitcnt lgkmcnt(1)
	v_mfma_f32_32x32x16_bf16 v[50:65], v[78:81], v[82:85], v[50:65]
	v_mul_f32_e32 v2, v14, v76
	v_mul_f32_e32 v3, v15, v76
	v_mul_f32_e32 v8, v16, v76
	v_mul_f32_e32 v9, v17, v76
	v_mul_f32_e32 v14, v26, v104
	v_mul_f32_e32 v15, v27, v104
	v_cvt_pk_bf16_f32 v77, v8, v9
	v_cvt_pk_bf16_f32 v76, v2, v3
	v_cvt_pk_bf16_f32 v74, v10, v11
	v_pk_mul_f32 v[2:3], v[28:29], v[104:105] op_sel_hi:[1,0]
	v_mfma_f32_32x32x16_bf16 v[34:49], v[78:81], v[96:99], v[34:49]
	v_mul_f32_e32 v8, v30, v104
	v_mul_f32_e32 v9, v31, v104
	v_mul_f32_e32 v10, v32, v104
	v_mul_f32_e32 v11, v33, v104
	v_cvt_pk_bf16_f32 v75, v12, v13
	v_cvt_pk_bf16_f32 v81, v10, v11
	v_cvt_pk_bf16_f32 v80, v8, v9
	v_cvt_pk_bf16_f32 v79, v2, v3
	v_cvt_pk_bf16_f32 v78, v14, v15
	s_waitcnt lgkmcnt(0)
	v_mfma_f32_32x32x16_bf16 v[50:65], v[86:89], v[74:77], v[50:65]
	v_mfma_f32_32x32x16_bf16 v[34:49], v[86:89], v[78:81], v[34:49]
	ds_read_b128 v[86:89], v150 offset:56320
	ds_read_b128 v[18:21], v150 offset:44032
	ds_read_b128 v[22:25], v150 offset:45056
	ds_read_b128 v[26:29], v150 offset:46080
	ds_read_b128 v[30:33], v150 offset:47104
	ds_read_b128 v[100:103], v150 offset:57344
	s_waitcnt lgkmcnt(1)
	v_mfma_f32_32x32x16_bf16 v[18:33], v[86:89], v[4:7], v[18:33]
	ds_read_b128 v[2:5], v150 offset:48128
	ds_read_b128 v[6:9], v150 offset:49152
	ds_read_b128 v[10:13], v150 offset:50176
	ds_read_b128 v[14:17], v150 offset:51200
	s_waitcnt lgkmcnt(0)
	v_mfma_f32_32x32x16_bf16 v[2:17], v[86:89], v[92:95], v[2:17]
	v_mfma_f32_32x32x16_bf16 v[18:33], v[100:103], v[70:73], v[18:33]
	v_mfma_f32_32x32x16_bf16 v[2:17], v[100:103], v[66:69], v[2:17]
	ds_read_b128 v[66:69], v150 offset:58368
	ds_read_b128 v[70:73], v150 offset:59392
	s_waitcnt lgkmcnt(1)
	v_mfma_f32_32x32x16_bf16 v[18:33], v[66:69], v[82:85], v[18:33]
	v_mfma_f32_32x32x16_bf16 v[2:17], v[66:69], v[96:99], v[2:17]
	s_waitcnt lgkmcnt(0)
	v_mfma_f32_32x32x16_bf16 v[18:33], v[70:73], v[74:77], v[18:33]
	v_mfma_f32_32x32x16_bf16 v[2:17], v[70:73], v[78:81], v[2:17]
	s_nop 10
	v_mul_f32_e32 v66, v22, v22
	v_mul_f32_e32 v67, v23, v23
	v_mul_f32_e32 v68, v30, v30
	v_mul_f32_e32 v69, v31, v31
	v_mul_f32_e32 v70, v24, v24
	v_mul_f32_e32 v71, v25, v25
	v_pk_mul_f32 v[72:73], v[32:33], v[32:33]
	v_pk_mul_f32 v[74:75], v[20:21], v[20:21]
	v_pk_mul_f32 v[76:77], v[28:29], v[28:29]
	v_pk_mul_f32 v[78:79], v[26:27], v[26:27]
	v_pk_mul_f32 v[80:81], v[18:19], v[18:19]
	v_pk_fma_f32 v[78:79], v[58:59], v[58:59], v[78:79]
	v_pk_fma_f32 v[76:77], v[60:61], v[60:61], v[76:77]
	v_pk_fma_f32 v[74:75], v[52:53], v[52:53], v[74:75]
	v_pk_fma_f32 v[72:73], v[64:65], v[64:65], v[72:73]
	v_pk_fma_f32 v[70:71], v[56:57], v[56:57], v[70:71]
	v_pk_fma_f32 v[68:69], v[62:63], v[62:63], v[68:69]
	v_pk_fma_f32 v[66:67], v[54:55], v[54:55], v[66:67]
	v_pk_fma_f32 v[80:81], v[50:51], v[50:51], v[80:81]
	v_pk_add_f32 v[66:67], v[66:67], v[68:69]
	v_pk_add_f32 v[68:69], v[70:71], v[72:73]
	v_pk_add_f32 v[70:71], v[74:75], v[76:77]
	v_pk_add_f32 v[72:73], v[80:81], v[78:79]
	v_pk_add_f32 v[68:69], v[70:71], v[68:69]
	v_pk_add_f32 v[66:67], v[72:73], v[66:67]
	v_pk_mul_f32 v[72:73], v[14:15], v[14:15]
	v_pk_mov_b32 v[70:71], v[66:67], v[68:69] op_sel:[1,0]
	v_mov_b32_e32 v67, v69
	v_pk_add_f32 v[66:67], v[70:71], v[66:67]
	v_pk_mul_f32 v[70:71], v[6:7], v[6:7]
	v_pk_mul_f32 v[74:75], v[8:9], v[8:9]
	v_pk_mul_f32 v[76:77], v[16:17], v[16:17]
	v_pk_mul_f32 v[78:79], v[4:5], v[4:5]
	v_pk_mul_f32 v[80:81], v[12:13], v[12:13]
	v_pk_mul_f32 v[82:83], v[10:11], v[10:11]
	v_pk_mul_f32 v[84:85], v[2:3], v[2:3]
	v_pk_fma_f32 v[82:83], v[42:43], v[42:43], v[82:83]
	v_pk_fma_f32 v[80:81], v[44:45], v[44:45], v[80:81]
	v_pk_fma_f32 v[78:79], v[36:37], v[36:37], v[78:79]
	v_pk_fma_f32 v[76:77], v[48:49], v[48:49], v[76:77]
	v_pk_fma_f32 v[74:75], v[40:41], v[40:41], v[74:75]
	v_pk_fma_f32 v[72:73], v[46:47], v[46:47], v[72:73]
	v_pk_fma_f32 v[70:71], v[38:39], v[38:39], v[70:71]
	v_pk_fma_f32 v[84:85], v[34:35], v[34:35], v[84:85]
	v_pk_add_f32 v[70:71], v[70:71], v[72:73]
	v_pk_add_f32 v[72:73], v[74:75], v[76:77]
	v_pk_add_f32 v[74:75], v[78:79], v[80:81]
	v_pk_add_f32 v[76:77], v[84:85], v[82:83]
	v_pk_add_f32 v[72:73], v[74:75], v[72:73]
	v_pk_add_f32 v[70:71], v[76:77], v[70:71]
	v_pk_add_f32 v[66:67], v[66:67], v[66:67] op_sel:[0,1] op_sel_hi:[1,0]
	v_pk_mov_b32 v[74:75], v[70:71], v[72:73] op_sel:[1,0]
	v_mov_b32_e32 v71, v73
	v_pk_add_f32 v[70:71], v[74:75], v[70:71]
	v_mov_b32_e32 v69, v66
	v_pk_add_f32 v[70:71], v[70:71], v[70:71] op_sel:[0,1] op_sel_hi:[1,0]
	s_nop 0
	v_permlane32_swap_b32_e32 v66, v69
	v_mov_b32_e32 v68, v70
	s_nop 1
	v_permlane32_swap_b32_e32 v70, v68
	v_mov_b32_e32 v71, v66
	v_pk_add_f32 v[66:67], v[70:71], v[68:69]
	v_pk_fma_f32 v[66:67], v[66:67], s[0:1], v[152:153] op_sel_hi:[1,0,0]
	s_mov_b32 s1, 0x800000
	v_mul_f32_e32 v68, 0x4b800000, v67
	v_cmp_gt_f32_e32 vcc, s1, v67
	s_nop 1
	v_cndmask_b32_e32 v67, v67, v68, vcc
	v_rsq_f32_e32 v67, v67
	s_nop 0
	v_mul_f32_e32 v68, 0x45800000, v67
	v_cndmask_b32_e32 v68, v67, v68, vcc
	v_pk_mul_f32 v[158:159], v[50:51], v[68:69] op_sel_hi:[1,0]
	v_pk_mul_f32 v[50:51], v[18:19], v[68:69] op_sel_hi:[1,0]
	v_mul_f32_e32 v18, 0x4b800000, v66
	v_cmp_gt_f32_e32 vcc, s1, v66
	v_pk_mul_f32 v[80:81], v[60:61], v[68:69] op_sel_hi:[1,0]
	v_pk_mul_f32 v[60:61], v[28:29], v[68:69] op_sel_hi:[1,0]
	v_cndmask_b32_e32 v18, v66, v18, vcc
	v_rsq_f32_e32 v18, v18
	v_pk_mul_f32 v[78:79], v[58:59], v[68:69] op_sel_hi:[1,0]
	v_pk_mul_f32 v[160:161], v[52:53], v[68:69] op_sel_hi:[1,0]
	v_pk_mul_f32 v[82:83], v[54:55], v[68:69] op_sel_hi:[1,0]
	v_mul_f32_e32 v19, 0x45800000, v18
	v_cndmask_b32_e32 v28, v18, v19, vcc
	v_pk_mul_f32 v[168:169], v[56:57], v[68:69] op_sel_hi:[1,0]
	v_pk_mul_f32 v[58:59], v[26:27], v[68:69] op_sel_hi:[1,0]
	v_pk_mul_f32 v[52:53], v[20:21], v[68:69] op_sel_hi:[1,0]
	v_pk_mul_f32 v[54:55], v[22:23], v[68:69] op_sel_hi:[1,0]
	v_pk_mul_f32 v[56:57], v[24:25], v[68:69] op_sel_hi:[1,0]
	v_pk_mul_f32 v[18:19], v[42:43], v[28:29] op_sel_hi:[1,0]
	v_pk_mul_f32 v[20:21], v[44:45], v[28:29] op_sel_hi:[1,0]
	v_pk_mul_f32 v[22:23], v[46:47], v[28:29] op_sel_hi:[1,0]
	v_pk_mul_f32 v[26:27], v[48:49], v[28:29] op_sel_hi:[1,0]
	v_pk_mul_f32 v[162:163], v[34:35], v[28:29] op_sel_hi:[1,0]
	v_pk_mul_f32 v[164:165], v[36:37], v[28:29] op_sel_hi:[1,0]
	v_pk_mul_f32 v[166:167], v[38:39], v[28:29] op_sel_hi:[1,0]
	v_pk_mul_f32 v[24:25], v[40:41], v[28:29] op_sel_hi:[1,0]
	v_pk_mul_f32 v[104:105], v[2:3], v[28:29] op_sel_hi:[1,0]
	v_pk_mul_f32 v[112:113], v[4:5], v[28:29] op_sel_hi:[1,0]
	ds_read_b128 v[2:5], v150 offset:60416
	ds_read_b128 v[34:37], v174 offset:32768
	ds_read_b128 v[38:41], v174 offset:32800
	ds_read_b128 v[42:45], v174 offset:32832
	ds_read_b128 v[46:49], v174 offset:32864
	v_cvt_pk_bf16_f32 v129, v168, v169
	v_cvt_pk_bf16_f32 v128, v82, v83
	v_cvt_pk_bf16_f32 v127, v160, v161
	v_cvt_pk_bf16_f32 v126, v158, v159
	v_cvt_pk_bf16_f32 v137, v24, v25
	v_cvt_pk_bf16_f32 v136, v166, v167
	v_cvt_pk_bf16_f32 v135, v164, v165
	s_waitcnt lgkmcnt(0)
	v_mfma_f32_32x32x16_bf16 v[86:101], v[2:5], v[126:129], v[34:49]
	v_cvt_pk_bf16_f32 v134, v162, v163
	v_mul_f32_e32 v84, v62, v68
	v_mul_f32_e32 v85, v63, v68
	v_mul_f32_e32 v170, v64, v68
	v_mul_f32_e32 v171, v65, v68
	v_pk_mul_f32 v[62:63], v[30:31], v[68:69] op_sel_hi:[1,0]
	v_pk_mul_f32 v[64:65], v[32:33], v[68:69] op_sel_hi:[1,0]
	v_pk_mul_f32 v[116:117], v[6:7], v[28:29] op_sel_hi:[1,0]
	v_pk_mul_f32 v[154:155], v[8:9], v[28:29] op_sel_hi:[1,0]
	v_mfma_f32_32x32x16_bf16 v[34:49], v[2:5], v[134:137], v[34:49]
	ds_read_b128 v[6:9], v150 offset:61440
	ds_read_b128 v[66:69], v174 offset:32896
	ds_read_b128 v[106:109], v150 offset:64512
	v_cvt_pk_bf16_f32 v125, v170, v171
	v_cvt_pk_bf16_f32 v124, v84, v85
	v_cvt_pk_bf16_f32 v123, v80, v81
	v_cvt_pk_bf16_f32 v122, v78, v79
	v_cvt_pk_bf16_f32 v149, v26, v27
	v_cvt_pk_bf16_f32 v148, v22, v23
	v_cvt_pk_bf16_f32 v147, v20, v21
	v_cvt_pk_bf16_f32 v146, v18, v19
	s_waitcnt lgkmcnt(2)
	v_mfma_f32_32x32x16_bf16 v[86:101], v[6:9], v[122:125], v[86:101]
	v_mul_f32_e32 v102, v10, v28
	v_mul_f32_e32 v103, v11, v28
	v_mul_f32_e32 v110, v12, v28
	v_mul_f32_e32 v111, v13, v28
	v_mul_f32_e32 v114, v14, v28
	v_mul_f32_e32 v115, v15, v28
	v_pk_mul_f32 v[156:157], v[16:17], v[28:29] op_sel_hi:[1,0]
	ds_read_b128 v[176:179], v174 offset:33536
	ds_read_b128 v[180:183], v174 offset:33568
	ds_read_b128 v[184:187], v174 offset:33600
	ds_read_b128 v[28:31], v174 offset:33632
	ds_read_b128 v[188:191], v174 offset:33792
	ds_read_b128 v[192:195], v174 offset:33824
	ds_read_b128 v[196:199], v174 offset:33856
	ds_read_b128 v[200:203], v174 offset:33888
	ds_read_b128 v[204:207], v150 offset:62464
	v_cvt_pk_bf16_f32 v133, v56, v57
	v_mfma_f32_32x32x16_bf16 v[34:49], v[6:9], v[146:149], v[34:49]
	v_cvt_pk_bf16_f32 v132, v54, v55
	v_cvt_pk_bf16_f32 v131, v52, v53
	v_cvt_pk_bf16_f32 v130, v50, v51
	ds_read_b128 v[70:73], v174 offset:33664
	ds_read_b128 v[74:77], v174 offset:33920
	ds_read_b128 v[208:211], v150 offset:63488
	v_cvt_pk_bf16_f32 v145, v154, v155
	v_cvt_pk_bf16_f32 v144, v116, v117
	v_cvt_pk_bf16_f32 v143, v112, v113
	v_cvt_pk_bf16_f32 v142, v104, v105
	s_waitcnt lgkmcnt(3)
	v_mfma_f32_32x32x16_bf16 v[86:101], v[204:207], v[130:133], v[86:101]
	v_cvt_pk_bf16_f32 v121, v64, v65
	v_cvt_pk_bf16_f32 v120, v62, v63
	v_cvt_pk_bf16_f32 v119, v60, v61
	v_cvt_pk_bf16_f32 v118, v58, v59
	v_cvt_pk_bf16_f32 v141, v156, v157
	v_cvt_pk_bf16_f32 v140, v114, v115
	v_cvt_pk_bf16_f32 v139, v110, v111
	v_mfma_f32_32x32x16_bf16 v[34:49], v[204:207], v[142:145], v[34:49]
	v_cvt_pk_bf16_f32 v138, v102, v103
	v_fma_f32 v16, v30, v170, v202
	v_fma_f32 v17, v31, v171, v203
	v_fma_f32 v14, v28, v84, v200
	v_fma_f32 v15, v29, v85, v201
	v_pk_fma_f32 v[12:13], v[186:187], v[80:81], v[198:199]
	v_pk_fma_f32 v[10:11], v[184:185], v[78:79], v[196:197]
	v_pk_fma_f32 v[8:9], v[182:183], v[168:169], v[194:195]
	s_waitcnt lgkmcnt(0)
	v_mfma_f32_32x32x16_bf16 v[86:101], v[208:211], v[118:121], v[86:101]
	v_fma_f32 v6, v180, v82, v192
	v_fma_f32 v7, v181, v83, v193
	ds_read_b128 v[78:81], v174 offset:33760
	ds_read_b128 v[82:85], v174 offset:33248
	v_fma_f32 v4, v178, v160, v190
	v_fma_f32 v5, v179, v161, v191
	v_pk_fma_f32 v[2:3], v[176:177], v[158:159], v[188:189]
	v_pk_fma_f32 v[32:33], v[30:31], v[26:27], v[202:203]
	v_pk_fma_f32 v[30:31], v[28:29], v[22:23], v[200:201]
	v_pk_fma_f32 v[28:29], v[186:187], v[20:21], v[198:199]
	v_pk_fma_f32 v[26:27], v[184:185], v[18:19], v[196:197]
	v_pk_fma_f32 v[24:25], v[182:183], v[24:25], v[194:195]
	v_pk_fma_f32 v[22:23], v[180:181], v[166:167], v[192:193]
	v_pk_fma_f32 v[20:21], v[178:179], v[164:165], v[190:191]
	v_pk_fma_f32 v[18:19], v[176:177], v[162:163], v[188:189]
	ds_read_b128 v[158:161], v174 offset:33696
	ds_read_b128 v[162:165], v174 offset:33728
	ds_read_b128 v[166:169], v174 offset:33952
	ds_read_b128 v[176:179], v174 offset:33984
	ds_read_b128 v[180:183], v174 offset:34016
	ds_read_b128 v[184:187], v212 offset:11264
	v_mfma_f32_32x32x16_bf16 v[34:49], v[208:211], v[138:141], v[34:49]
	v_cvt_pk_bf16_f32 v86, v86, v87
	v_cvt_pk_bf16_f32 v87, v88, v89
	v_cvt_pk_bf16_f32 v88, v90, v91
	v_cvt_pk_bf16_f32 v89, v92, v93
	ds_read_b128 v[90:93], v212 offset:12288
	v_pk_max_i16 v86, v86, 0
	v_pk_max_i16 v87, v87, 0
	v_pk_max_i16 v88, v88, 0
	v_pk_max_i16 v89, v89, 0
	s_nop 1
	s_nop 0
	v_cvt_pk_bf16_f32 v188, v34, v35
	v_cvt_pk_bf16_f32 v189, v36, v37
	v_cvt_pk_bf16_f32 v190, v38, v39
	v_cvt_pk_bf16_f32 v191, v40, v41
	s_waitcnt lgkmcnt(1)
	v_mfma_f32_32x32x16_bf16 v[2:17], v[184:187], v[86:89], v[2:17]
	v_pk_max_i16 v188, v188, 0
	v_pk_max_i16 v189, v189, 0
	v_pk_max_i16 v190, v190, 0
	v_pk_max_i16 v191, v191, 0
	v_cvt_pk_bf16_f32 v94, v94, v95
	v_cvt_pk_bf16_f32 v95, v96, v97
	v_cvt_pk_bf16_f32 v96, v98, v99
	v_cvt_pk_bf16_f32 v97, v100, v101
	v_cvt_pk_bf16_f32 v98, v42, v43
	v_cvt_pk_bf16_f32 v99, v44, v45
	v_mfma_f32_32x32x16_bf16 v[18:33], v[184:187], v[188:191], v[18:33]
	ds_read_b128 v[184:187], v212 offset:19456
	v_cvt_pk_bf16_f32 v100, v46, v47
	v_cvt_pk_bf16_f32 v101, v48, v49
	v_fma_f32 v64, v80, v64, v182
	v_fma_f32 v65, v81, v65, v183
	v_pk_fma_f32 v[62:63], v[78:79], v[62:63], v[180:181]
	v_pk_fma_f32 v[60:61], v[164:165], v[60:61], v[178:179]
	v_pk_fma_f32 v[58:59], v[162:163], v[58:59], v[176:177]
	v_pk_max_i16 v94, v94, 0
	v_pk_max_i16 v95, v95, 0
	v_pk_max_i16 v96, v96, 0
	v_pk_max_i16 v97, v97, 0
	v_pk_max_i16 v98, v98, 0
	v_pk_max_i16 v99, v99, 0
	v_pk_max_i16 v100, v100, 0
	v_pk_max_i16 v101, v101, 0
	v_pk_fma_f32 v[56:57], v[160:161], v[56:57], v[168:169]
	s_waitcnt lgkmcnt(1)
	v_mfma_f32_32x32x16_bf16 v[2:17], v[90:93], v[94:97], v[2:17]
	v_fma_f32 v54, v158, v54, v166
	v_fma_f32 v55, v159, v55, v167
	v_fma_f32 v52, v72, v52, v76
	v_fma_f32 v53, v73, v53, v77
	v_fma_f32 v50, v70, v50, v74
	v_fma_f32 v51, v71, v51, v75
	v_pk_fma_f32 v[48:49], v[80:81], v[156:157], v[182:183]
	v_pk_fma_f32 v[46:47], v[78:79], v[114:115], v[180:181]
	v_pk_fma_f32 v[44:45], v[164:165], v[110:111], v[178:179]
	v_pk_fma_f32 v[42:43], v[162:163], v[102:103], v[176:177]
	v_mfma_f32_32x32x16_bf16 v[18:33], v[90:93], v[98:101], v[18:33]
	ds_read_b128 v[90:93], v212 offset:20480
	v_fma_f32 v40, v160, v154, v168
	v_fma_f32 v41, v161, v155, v169
	v_fma_f32 v38, v158, v116, v166
	v_fma_f32 v39, v159, v117, v167
	v_pk_fma_f32 v[36:37], v[72:73], v[112:113], v[76:77]
	v_pk_fma_f32 v[34:35], v[70:71], v[104:105], v[74:75]
	s_waitcnt lgkmcnt(1)
	v_mfma_f32_32x32x16_bf16 v[50:65], v[184:187], v[86:89], v[50:65]
	ds_read_b128 v[70:73], v174 offset:32928
	ds_read_b128 v[74:77], v174 offset:32960
	ds_read_b128 v[78:81], v174 offset:32992
	ds_read_b128 v[86:89], v174 offset:33024
	ds_read_b128 v[110:113], v212 offset:1024
	v_mfma_f32_32x32x16_bf16 v[34:49], v[184:187], v[188:191], v[34:49]
	s_waitcnt lgkmcnt(5)
	v_mfma_f32_32x32x16_bf16 v[50:65], v[90:93], v[94:97], v[50:65]
	v_mfma_f32_32x32x16_bf16 v[34:49], v[90:93], v[98:101], v[34:49]
	s_waitcnt lgkmcnt(2)
	v_mfma_f32_32x32x16_bf16 v[90:105], v[106:109], v[126:129], v[66:81]
	v_mfma_f32_32x32x16_bf16 v[66:81], v[106:109], v[134:137], v[66:81]
	ds_read_b128 v[106:109], v212 offset:0
	s_waitcnt lgkmcnt(0)
	v_mfma_f32_32x32x16_bf16 v[90:105], v[106:109], v[122:125], v[90:105]
	v_mfma_f32_32x32x16_bf16 v[66:81], v[106:109], v[146:149], v[66:81]
	ds_read_b128 v[106:109], v212 offset:2048
	v_mfma_f32_32x32x16_bf16 v[90:105], v[110:113], v[130:133], v[90:105]
	v_mfma_f32_32x32x16_bf16 v[66:81], v[110:113], v[142:145], v[66:81]
	ds_read_b128 v[110:113], v212 offset:13312
	s_waitcnt lgkmcnt(1)
	v_mfma_f32_32x32x16_bf16 v[90:105], v[106:109], v[118:121], v[90:105]
	v_mfma_f32_32x32x16_bf16 v[66:81], v[106:109], v[138:141], v[66:81]
	s_nop 10
	v_cvt_pk_bf16_f32 v90, v90, v91
	v_cvt_pk_bf16_f32 v91, v92, v93
	v_cvt_pk_bf16_f32 v92, v94, v95
	v_cvt_pk_bf16_f32 v94, v98, v99
	v_cvt_pk_bf16_f32 v95, v100, v101
	ds_read_b128 v[98:101], v212 offset:21504
	v_cvt_pk_bf16_f32 v66, v66, v67
	v_cvt_pk_bf16_f32 v67, v68, v69
	v_cvt_pk_bf16_f32 v68, v70, v71
	v_cvt_pk_bf16_f32 v93, v96, v97
	v_cvt_pk_bf16_f32 v69, v72, v73
	ds_read_b128 v[70:73], v212 offset:14336
	v_pk_max_i16 v90, v90, 0
	v_pk_max_i16 v91, v91, 0
	v_pk_max_i16 v92, v92, 0
	v_pk_max_i16 v93, v93, 0
	v_pk_max_i16 v66, v66, 0
	v_pk_max_i16 v67, v67, 0
	v_pk_max_i16 v68, v68, 0
	v_pk_max_i16 v69, v69, 0
	v_cvt_pk_bf16_f32 v96, v102, v103
	s_waitcnt lgkmcnt(2)
	v_mfma_f32_32x32x16_bf16 v[2:17], v[110:113], v[90:93], v[2:17]
	v_cvt_pk_bf16_f32 v97, v104, v105
	v_cvt_pk_bf16_f32 v74, v74, v75
	v_cvt_pk_bf16_f32 v75, v76, v77
	v_cvt_pk_bf16_f32 v76, v78, v79
	v_cvt_pk_bf16_f32 v77, v80, v81
	v_pk_max_i16 v94, v94, 0
	v_pk_max_i16 v95, v95, 0
	v_pk_max_i16 v96, v96, 0
	v_pk_max_i16 v97, v97, 0
	v_pk_max_i16 v74, v74, 0
	v_pk_max_i16 v75, v75, 0
	v_pk_max_i16 v76, v76, 0
	v_pk_max_i16 v77, v77, 0
	v_mfma_f32_32x32x16_bf16 v[18:33], v[110:113], v[66:69], v[18:33]
	s_waitcnt lgkmcnt(1)
	v_mfma_f32_32x32x16_bf16 v[34:49], v[98:101], v[66:69], v[34:49]
	ds_read_b128 v[66:69], v212 offset:22528
	v_mfma_f32_32x32x16_bf16 v[50:65], v[98:101], v[90:93], v[50:65]
	s_waitcnt lgkmcnt(1)
	v_mfma_f32_32x32x16_bf16 v[2:17], v[70:73], v[94:97], v[2:17]
	v_mfma_f32_32x32x16_bf16 v[18:33], v[70:73], v[74:77], v[18:33]
	ds_read_b128 v[78:81], v212 offset:3072
	s_waitcnt lgkmcnt(1)
	v_mfma_f32_32x32x16_bf16 v[50:65], v[66:69], v[94:97], v[50:65]
	ds_read_b128 v[90:93], v174 offset:33056
	ds_read_b128 v[94:97], v174 offset:33088
	ds_read_b128 v[98:101], v174 offset:33120
	ds_read_b128 v[70:73], v174 offset:33152
	v_mfma_f32_32x32x16_bf16 v[34:49], v[66:69], v[74:77], v[34:49]
	ds_read_b128 v[66:69], v212 offset:4096
	ds_read_b128 v[74:77], v212 offset:5120
	s_waitcnt lgkmcnt(3)
	v_mfma_f32_32x32x16_bf16 v[102:117], v[78:81], v[126:129], v[86:101]
	v_mfma_f32_32x32x16_bf16 v[86:101], v[78:81], v[134:137], v[86:101]
	s_waitcnt lgkmcnt(1)
	v_mfma_f32_32x32x16_bf16 v[86:101], v[66:69], v[146:149], v[86:101]
	v_mfma_f32_32x32x16_bf16 v[102:117], v[66:69], v[122:125], v[102:117]
	ds_read_b128 v[66:69], v212 offset:6144
	s_waitcnt lgkmcnt(1)
	v_mfma_f32_32x32x16_bf16 v[86:101], v[74:77], v[142:145], v[86:101]
	v_mfma_f32_32x32x16_bf16 v[102:117], v[74:77], v[130:133], v[102:117]
	ds_read_b128 v[74:77], v212 offset:15360
	s_waitcnt lgkmcnt(1)
	v_mfma_f32_32x32x16_bf16 v[86:101], v[66:69], v[138:141], v[86:101]
	v_mfma_f32_32x32x16_bf16 v[102:117], v[66:69], v[118:121], v[102:117]
	s_nop 10
	v_cvt_pk_bf16_f32 v78, v86, v87
	v_cvt_pk_bf16_f32 v80, v90, v91
	v_cvt_pk_bf16_f32 v79, v88, v89
	v_cvt_pk_bf16_f32 v81, v92, v93
	ds_read_b128 v[86:89], v212 offset:16384
	ds_read_b128 v[90:93], v212 offset:23552
	v_cvt_pk_bf16_f32 v66, v102, v103
	v_cvt_pk_bf16_f32 v67, v104, v105
	v_cvt_pk_bf16_f32 v68, v106, v107
	v_cvt_pk_bf16_f32 v69, v108, v109
	v_pk_max_i16 v66, v66, 0
	v_pk_max_i16 v67, v67, 0
	v_pk_max_i16 v68, v68, 0
	v_pk_max_i16 v69, v69, 0
	v_pk_max_i16 v78, v78, 0
	v_pk_max_i16 v79, v79, 0
	v_pk_max_i16 v80, v80, 0
	v_pk_max_i16 v81, v81, 0
	v_cvt_pk_bf16_f32 v94, v94, v95
	s_waitcnt lgkmcnt(2)
	v_mfma_f32_32x32x16_bf16 v[18:33], v[74:77], v[78:81], v[18:33]
	v_cvt_pk_bf16_f32 v95, v96, v97
	v_cvt_pk_bf16_f32 v96, v98, v99
	v_cvt_pk_bf16_f32 v97, v100, v101
	v_pk_max_i16 v94, v94, 0
	v_pk_max_i16 v95, v95, 0
	v_pk_max_i16 v96, v96, 0
	v_pk_max_i16 v97, v97, 0
	v_mfma_f32_32x32x16_bf16 v[2:17], v[74:77], v[66:69], v[2:17]
	v_cvt_pk_bf16_f32 v74, v110, v111
	v_cvt_pk_bf16_f32 v75, v112, v113
	v_cvt_pk_bf16_f32 v76, v114, v115
	v_cvt_pk_bf16_f32 v77, v116, v117
	v_pk_max_i16 v74, v74, 0
	v_pk_max_i16 v75, v75, 0
	v_pk_max_i16 v76, v76, 0
	v_pk_max_i16 v77, v77, 0
	s_waitcnt lgkmcnt(0)
	v_mfma_f32_32x32x16_bf16 v[50:65], v[90:93], v[66:69], v[50:65]
	ds_read_b128 v[66:69], v212 offset:24576
	v_mfma_f32_32x32x16_bf16 v[34:49], v[90:93], v[78:81], v[34:49]
	ds_read_b128 v[102:105], v212 offset:7168
	v_mfma_f32_32x32x16_bf16 v[2:17], v[86:89], v[74:77], v[2:17]
	s_waitcnt lgkmcnt(1)
	v_mfma_f32_32x32x16_bf16 v[50:65], v[66:69], v[74:77], v[50:65]
	ds_read_b128 v[74:77], v174 offset:33184
	ds_read_b128 v[78:81], v174 offset:33216
	v_mfma_f32_32x32x16_bf16 v[34:49], v[66:69], v[94:97], v[34:49]
	ds_read_b128 v[66:69], v212 offset:8192
	v_mfma_f32_32x32x16_bf16 v[18:33], v[86:89], v[94:97], v[18:33]
	s_waitcnt lgkmcnt(1)
	v_mfma_f32_32x32x16_bf16 v[86:101], v[102:105], v[126:129], v[70:85]
	v_mfma_f32_32x32x16_bf16 v[70:85], v[102:105], v[134:137], v[70:85]
	ds_read_b128 v[102:105], v212 offset:9216
	v_lshlrev_b32_e32 v135, 2, v1
	v_add_u32_e32 v134, v172, v174
	s_waitcnt lgkmcnt(1)
	v_mfma_f32_32x32x16_bf16 v[86:101], v[66:69], v[122:125], v[86:101]
	v_mfma_f32_32x32x16_bf16 v[70:85], v[66:69], v[146:149], v[70:85]
	ds_read_b128 v[66:69], v212 offset:10240
	s_waitcnt lgkmcnt(1)
	v_mfma_f32_32x32x16_bf16 v[86:101], v[102:105], v[130:133], v[86:101]
	v_mfma_f32_32x32x16_bf16 v[70:85], v[102:105], v[142:145], v[70:85]
	ds_read_b128 v[102:105], v212 offset:17408
	s_waitcnt lgkmcnt(1)
	v_mfma_f32_32x32x16_bf16 v[86:101], v[66:69], v[118:121], v[86:101]
	v_mfma_f32_32x32x16_bf16 v[70:85], v[66:69], v[138:141], v[70:85]
	s_nop 10
	v_cvt_pk_bf16_f32 v68, v90, v91
	v_cvt_pk_bf16_f32 v69, v92, v93
	ds_read_b128 v[90:93], v212 offset:25600
	v_cvt_pk_bf16_f32 v66, v86, v87
	v_cvt_pk_bf16_f32 v67, v88, v89
	v_pk_max_i16 v66, v66, 0
	v_pk_max_i16 v67, v67, 0
	v_pk_max_i16 v68, v68, 0
	v_pk_max_i16 v69, v69, 0
	v_cvt_pk_bf16_f32 v70, v70, v71
	v_cvt_pk_bf16_f32 v71, v72, v73
	s_waitcnt lgkmcnt(1)
	v_mfma_f32_32x32x16_bf16 v[2:17], v[102:105], v[66:69], v[2:17]
	v_cvt_pk_bf16_f32 v72, v74, v75
	v_cvt_pk_bf16_f32 v73, v76, v77
	ds_read_b128 v[74:77], v212 offset:18432
	v_cvt_pk_bf16_f32 v86, v94, v95
	v_cvt_pk_bf16_f32 v87, v96, v97
	v_cvt_pk_bf16_f32 v88, v98, v99
	s_waitcnt lgkmcnt(1)
	v_mfma_f32_32x32x16_bf16 v[50:65], v[90:93], v[66:69], v[50:65]
	ds_read_b128 v[66:69], v212 offset:26624
	v_cvt_pk_bf16_f32 v89, v100, v101
	v_pk_max_i16 v86, v86, 0
	v_pk_max_i16 v87, v87, 0
	v_pk_max_i16 v88, v88, 0
	v_pk_max_i16 v89, v89, 0
	v_pk_max_i16 v70, v70, 0
	v_pk_max_i16 v71, v71, 0
	v_pk_max_i16 v72, v72, 0
	v_pk_max_i16 v73, v73, 0
	v_cvt_pk_bf16_f32 v78, v78, v79
	v_cvt_pk_bf16_f32 v79, v80, v81
	s_waitcnt lgkmcnt(1)
	v_mfma_f32_32x32x16_bf16 v[2:17], v[74:77], v[86:89], v[2:17]
	v_cvt_pk_bf16_f32 v80, v82, v83
	v_cvt_pk_bf16_f32 v81, v84, v85
	v_pk_max_i16 v78, v78, 0
	v_pk_max_i16 v79, v79, 0
	v_pk_max_i16 v80, v80, 0
	v_pk_max_i16 v81, v81, 0
	s_waitcnt lgkmcnt(0)
	v_mfma_f32_32x32x16_bf16 v[50:65], v[66:69], v[86:89], v[50:65]
	v_mfma_f32_32x32x16_bf16 v[34:49], v[90:93], v[70:73], v[34:49]
	s_nop 10
	v_add_f32_e32 v130, v10, v58
	v_add_f32_e32 v131, v11, v59
	v_add_f32_e32 v132, v12, v60
	v_add_f32_e32 v133, v13, v61
	v_add_f32_e32 v138, v4, v52
	v_add_f32_e32 v139, v5, v53
	v_pk_add_f32 v[140:141], v[16:17], v[64:65]
	v_pk_add_f32 v[142:143], v[8:9], v[56:57]
	v_pk_add_f32 v[144:145], v[14:15], v[62:63]
	v_pk_add_f32 v[146:147], v[6:7], v[54:55]
	v_mfma_f32_32x32x16_bf16 v[18:33], v[102:105], v[70:73], v[18:33]
	ds_read2st64_b32 v[70:71], v135 offset0:133 offset1:134
	v_add_f32_e32 v148, v2, v50
	v_add_f32_e32 v149, v3, v51
	v_add_f32_e32 v144, v146, v144
	v_add_f32_e32 v145, v147, v145
	v_pk_add_f32 v[140:141], v[142:143], v[140:141]
	v_pk_add_f32 v[132:133], v[138:139], v[132:133]
	v_pk_add_f32 v[130:131], v[148:149], v[130:131]
	v_pk_add_f32 v[132:133], v[132:133], v[140:141]
	v_pk_add_f32 v[130:131], v[130:131], v[144:145]
	v_mfma_f32_32x32x16_bf16 v[34:49], v[66:69], v[78:81], v[34:49]
	v_pk_mov_b32 v[138:139], v[130:131], v[132:133] op_sel:[1,0]
	v_mov_b32_e32 v131, v133
	s_waitcnt vmcnt(0) lgkmcnt(0)
	v_mul_f32_e32 v66, v175, v70
	v_pk_add_f32 v[130:131], v[138:139], v[130:131]
	ds_write_b32 v173, v66 offset:512
	v_mul_f32_e32 v66, v175, v71
	v_pk_add_f32 v[130:131], v[130:131], v[130:131] op_sel:[0,1] op_sel_hi:[1,0]
	s_waitcnt lgkmcnt(0)
	ds_read_b128 v[102:105], v174 offset:34560
	ds_read_b128 v[98:101], v174 offset:34592
	ds_read_b128 v[110:113], v174 offset:34624
	ds_read_b128 v[106:109], v174 offset:34656
	ds_read_b128 v[114:117], v174 offset:34688
	ds_read_b128 v[122:125], v174 offset:34720
	ds_read_b128 v[118:121], v174 offset:34752
	ds_read_b128 v[126:129], v174 offset:34784
	v_mov_b32_dpp v66, v66 quad_perm:[1,0,3,2] row_mask:0xf bank_mask:0xf bound_ctrl:1
	v_mov_b32_e32 v131, v130
	v_fmac_f32_e32 v66, v175, v71
	s_nop 0
	v_permlane32_swap_b32_e32 v130, v131
	v_add_f32_dpp v66, v66, v66 quad_perm:[2,3,0,1] row_mask:0xf bank_mask:0xf bound_ctrl:1
	v_add_f32_e32 v130, v130, v131
	v_fmamk_f32 v65, v130, 0xbc800000, v65
	v_add_f32_dpp v66, v66, v66 row_half_mirror row_mask:0xf bank_mask:0xf bound_ctrl:1
	v_fmamk_f32 v64, v130, 0xbc800000, v64
	v_fmamk_f32 v63, v130, 0xbc800000, v63
	v_fmamk_f32 v62, v130, 0xbc800000, v62
	v_fmamk_f32 v61, v130, 0xbc800000, v61
	v_fmamk_f32 v60, v130, 0xbc800000, v60
	v_fmamk_f32 v59, v130, 0xbc800000, v59
	v_fmamk_f32 v58, v130, 0xbc800000, v58
	v_fmamk_f32 v57, v130, 0xbc800000, v57
	v_fmamk_f32 v56, v130, 0xbc800000, v56
	v_fmamk_f32 v55, v130, 0xbc800000, v55
	v_fmamk_f32 v54, v130, 0xbc800000, v54
	v_fmamk_f32 v53, v130, 0xbc800000, v53
	v_fmamk_f32 v52, v130, 0xbc800000, v52
	v_fmamk_f32 v51, v130, 0xbc800000, v51
	v_fmac_f32_e32 v50, 0xbc800000, v130
	v_add_f32_dpp v66, v66, v66 row_ror:8 row_mask:0xf bank_mask:0xf bound_ctrl:1
	v_fmamk_f32 v17, v130, 0xbc800000, v17
	v_fmamk_f32 v16, v130, 0xbc800000, v16
	v_fmamk_f32 v15, v130, 0xbc800000, v15
	v_fmamk_f32 v14, v130, 0xbc800000, v14
	v_fmamk_f32 v13, v130, 0xbc800000, v13
	v_fmamk_f32 v12, v130, 0xbc800000, v12
	v_fmamk_f32 v11, v130, 0xbc800000, v11
	v_fmamk_f32 v10, v130, 0xbc800000, v10
	v_fmamk_f32 v9, v130, 0xbc800000, v9
	v_fmamk_f32 v8, v130, 0xbc800000, v8
	v_fmamk_f32 v7, v130, 0xbc800000, v7
	v_fmamk_f32 v6, v130, 0xbc800000, v6
	v_fmamk_f32 v5, v130, 0xbc800000, v5
	v_fmamk_f32 v4, v130, 0xbc800000, v4
	v_fmamk_f32 v3, v130, 0xbc800000, v3
	v_fmac_f32_e32 v2, 0xbc800000, v130
	v_pk_mul_f32 v[130:131], v[54:55], v[54:55]
	v_pk_mul_f32 v[132:133], v[62:63], v[62:63]
	v_pk_mul_f32 v[138:139], v[50:51], v[50:51]
	v_pk_mul_f32 v[140:141], v[58:59], v[58:59]
	v_pk_mul_f32 v[142:143], v[56:57], v[56:57]
	v_pk_mul_f32 v[144:145], v[64:65], v[64:65]
	v_pk_mul_f32 v[146:147], v[52:53], v[52:53]
	v_pk_mul_f32 v[148:149], v[60:61], v[60:61]
	v_mov_b32_e32 v67, v66
	v_pk_fma_f32 v[148:149], v[12:13], v[12:13], v[148:149]
	v_pk_fma_f32 v[146:147], v[4:5], v[4:5], v[146:147]
	v_pk_fma_f32 v[144:145], v[16:17], v[16:17], v[144:145]
	v_pk_fma_f32 v[142:143], v[8:9], v[8:9], v[142:143]
	v_pk_fma_f32 v[140:141], v[10:11], v[10:11], v[140:141]
	v_pk_fma_f32 v[138:139], v[2:3], v[2:3], v[138:139]
	v_pk_fma_f32 v[132:133], v[14:15], v[14:15], v[132:133]
	v_pk_fma_f32 v[130:131], v[6:7], v[6:7], v[130:131]
	v_permlane16_swap_b32_e32 v66, v67
	v_pk_add_f32 v[130:131], v[130:131], v[132:133]
	v_pk_add_f32 v[132:133], v[138:139], v[140:141]
	v_pk_add_f32 v[138:139], v[142:143], v[144:145]
	v_pk_add_f32 v[140:141], v[146:147], v[148:149]
	v_mfma_f32_32x32x16_bf16 v[18:33], v[74:77], v[78:81], v[18:33]
	v_add_f32_e32 v136, v66, v67
	ds_read_b128 v[70:73], v134 offset:512
	ds_read_b128 v[66:69], v134 offset:544
	ds_read_b128 v[78:81], v134 offset:576
	ds_read_b128 v[74:77], v134 offset:608
	ds_read_b128 v[82:85], v134 offset:640
	ds_read_b128 v[90:93], v134 offset:672
	ds_read_b128 v[86:89], v134 offset:704
	ds_read_b128 v[94:97], v134 offset:736
	v_pk_add_f32 v[138:139], v[140:141], v[138:139]
	v_pk_add_f32 v[130:131], v[132:133], v[130:131]
	s_waitcnt lgkmcnt(8)
	v_pk_mul_f32 v[140:141], v[126:127], v[62:63]
	v_pk_mov_b32 v[132:133], v[130:131], v[138:139] op_sel:[1,0]
	v_mov_b32_e32 v131, v139
	v_pk_mul_f32 v[138:139], v[122:123], v[54:55]
	v_pk_mul_f32 v[142:143], v[114:115], v[50:51]
	v_pk_mul_f32 v[144:145], v[118:119], v[58:59]
	v_pk_mul_f32 v[146:147], v[124:125], v[56:57]
	v_pk_mul_f32 v[148:149], v[128:129], v[64:65]
	v_pk_mul_f32 v[154:155], v[116:117], v[52:53]
	v_pk_mul_f32 v[156:157], v[120:121], v[60:61]
	v_pk_fma_f32 v[154:155], v[104:105], v[4:5], v[154:155]
	v_pk_fma_f32 v[156:157], v[112:113], v[12:13], v[156:157]
	v_pk_fma_f32 v[148:149], v[108:109], v[16:17], v[148:149]
	v_pk_fma_f32 v[146:147], v[100:101], v[8:9], v[146:147]
	v_pk_fma_f32 v[144:145], v[110:111], v[10:11], v[144:145]
	v_pk_fma_f32 v[142:143], v[102:103], v[2:3], v[142:143]
	v_pk_fma_f32 v[140:141], v[106:107], v[14:15], v[140:141]
	v_pk_fma_f32 v[138:139], v[98:99], v[6:7], v[138:139]
	v_pk_add_f32 v[130:131], v[132:133], v[130:131]
	v_pk_add_f32 v[138:139], v[138:139], v[140:141]
	v_pk_add_f32 v[140:141], v[142:143], v[144:145]
	v_pk_add_f32 v[142:143], v[146:147], v[148:149]
	v_pk_add_f32 v[144:145], v[154:155], v[156:157]
	v_pk_add_f32 v[132:133], v[130:131], v[130:131] op_sel:[0,1] op_sel_hi:[1,0]
	v_pk_add_f32 v[142:143], v[144:145], v[142:143]
	v_pk_add_f32 v[138:139], v[140:141], v[138:139]
	v_add_f32_e32 v133, v142, v143
	v_add_f32_e32 v130, v138, v139
	s_waitcnt lgkmcnt(2)
	v_pk_mul_f32 v[138:139], v[90:91], v[54:55]
	s_waitcnt lgkmcnt(0)
	v_pk_mul_f32 v[140:141], v[94:95], v[62:63]
	v_pk_mul_f32 v[142:143], v[82:83], v[50:51]
	v_pk_mul_f32 v[144:145], v[86:87], v[58:59]
	v_pk_mul_f32 v[146:147], v[92:93], v[56:57]
	v_pk_mul_f32 v[148:149], v[96:97], v[64:65]
	v_pk_mul_f32 v[154:155], v[84:85], v[52:53]
	v_pk_mul_f32 v[156:157], v[88:89], v[60:61]
	v_add_f32_e32 v130, v130, v133
	v_pk_fma_f32 v[156:157], v[80:81], v[12:13], v[156:157]
	v_pk_fma_f32 v[154:155], v[72:73], v[4:5], v[154:155]
	v_pk_fma_f32 v[148:149], v[76:77], v[16:17], v[148:149]
	v_pk_fma_f32 v[146:147], v[68:69], v[8:9], v[146:147]
	v_pk_fma_f32 v[144:145], v[78:79], v[10:11], v[144:145]
	v_pk_fma_f32 v[142:143], v[70:71], v[2:3], v[142:143]
	v_pk_fma_f32 v[140:141], v[74:75], v[14:15], v[140:141]
	v_pk_fma_f32 v[138:139], v[66:67], v[6:7], v[138:139]
	v_mov_b32_e32 v133, v130
	v_pk_add_f32 v[138:139], v[138:139], v[140:141]
	v_pk_add_f32 v[140:141], v[142:143], v[144:145]
	v_pk_add_f32 v[142:143], v[146:147], v[148:149]
	v_pk_add_f32 v[144:145], v[154:155], v[156:157]
	v_permlane32_swap_b32_e32 v130, v133
	v_pk_add_f32 v[142:143], v[144:145], v[142:143]
	v_add_f32_e32 v160, v130, v133
	v_pk_add_f32 v[138:139], v[140:141], v[138:139]
	v_add_f32_e32 v133, v142, v143
	v_pk_add_f32 v[140:141], v[26:27], v[42:43]
	v_pk_add_f32 v[142:143], v[28:29], v[44:45]
	v_pk_add_f32 v[144:145], v[20:21], v[36:37]
	v_pk_add_f32 v[146:147], v[32:33], v[48:49]
	v_pk_add_f32 v[148:149], v[24:25], v[40:41]
	v_pk_add_f32 v[154:155], v[30:31], v[46:47]
	v_pk_add_f32 v[156:157], v[22:23], v[38:39]
	v_pk_add_f32 v[158:159], v[18:19], v[34:35]
	v_pk_add_f32 v[154:155], v[156:157], v[154:155]
	v_pk_add_f32 v[146:147], v[148:149], v[146:147]
	v_pk_add_f32 v[142:143], v[144:145], v[142:143]
	v_pk_add_f32 v[140:141], v[158:159], v[140:141]
	v_pk_add_f32 v[142:143], v[142:143], v[146:147]
	v_pk_add_f32 v[140:141], v[140:141], v[154:155]
	v_add_f32_e32 v130, v138, v139
	v_pk_mov_b32 v[144:145], v[140:141], v[142:143] op_sel:[1,0]
	v_mov_b32_e32 v141, v143
	v_pk_add_f32 v[140:141], v[144:145], v[140:141]
	v_add_f32_e32 v133, v130, v133
	v_pk_add_f32 v[140:141], v[140:141], v[140:141] op_sel:[0,1] op_sel_hi:[1,0]
	v_mov_b32_e32 v131, v132
	v_mov_b32_e32 v130, v140
	s_nop 1
	v_permlane32_swap_b32_e32 v140, v130
	v_add_f32_e32 v130, v140, v130
	v_fmamk_f32 v49, v130, 0xbc800000, v49
	v_fmamk_f32 v48, v130, 0xbc800000, v48
	v_fmamk_f32 v47, v130, 0xbc800000, v47
	v_fmamk_f32 v46, v130, 0xbc800000, v46
	v_fmamk_f32 v45, v130, 0xbc800000, v45
	v_fmamk_f32 v44, v130, 0xbc800000, v44
	v_fmamk_f32 v43, v130, 0xbc800000, v43
	v_fmamk_f32 v42, v130, 0xbc800000, v42
	v_fmamk_f32 v41, v130, 0xbc800000, v41
	v_fmamk_f32 v40, v130, 0xbc800000, v40
	v_fmamk_f32 v39, v130, 0xbc800000, v39
	v_fmamk_f32 v38, v130, 0xbc800000, v38
	v_fmamk_f32 v37, v130, 0xbc800000, v37
	v_fmamk_f32 v36, v130, 0xbc800000, v36
	v_fmamk_f32 v35, v130, 0xbc800000, v35
	v_fmac_f32_e32 v34, 0xbc800000, v130
	v_fmamk_f32 v33, v130, 0xbc800000, v33
	v_fmamk_f32 v32, v130, 0xbc800000, v32
	v_fmamk_f32 v31, v130, 0xbc800000, v31
	v_fmamk_f32 v30, v130, 0xbc800000, v30
	v_fmamk_f32 v29, v130, 0xbc800000, v29
	v_fmamk_f32 v28, v130, 0xbc800000, v28
	v_fmamk_f32 v27, v130, 0xbc800000, v27
	v_fmamk_f32 v26, v130, 0xbc800000, v26
	v_fmamk_f32 v25, v130, 0xbc800000, v25
	v_fmamk_f32 v24, v130, 0xbc800000, v24
	v_fmamk_f32 v23, v130, 0xbc800000, v23
	v_fmamk_f32 v22, v130, 0xbc800000, v22
	v_fmamk_f32 v21, v130, 0xbc800000, v21
	v_fmamk_f32 v20, v130, 0xbc800000, v20
	v_fmamk_f32 v19, v130, 0xbc800000, v19
	v_fmac_f32_e32 v18, 0xbc800000, v130
	v_pk_mul_f32 v[140:141], v[38:39], v[38:39]
	v_pk_mul_f32 v[142:143], v[46:47], v[46:47]
	v_pk_mul_f32 v[144:145], v[34:35], v[34:35]
	v_pk_mul_f32 v[146:147], v[42:43], v[42:43]
	v_pk_mul_f32 v[148:149], v[40:41], v[40:41]
	v_pk_mul_f32 v[154:155], v[48:49], v[48:49]
	v_pk_mul_f32 v[156:157], v[36:37], v[36:37]
	v_pk_mul_f32 v[158:159], v[44:45], v[44:45]
	v_pk_fma_f32 v[156:157], v[20:21], v[20:21], v[156:157]
	v_pk_fma_f32 v[158:159], v[28:29], v[28:29], v[158:159]
	v_pk_fma_f32 v[154:155], v[32:33], v[32:33], v[154:155]
	v_pk_fma_f32 v[148:149], v[24:25], v[24:25], v[148:149]
	v_pk_fma_f32 v[146:147], v[26:27], v[26:27], v[146:147]
	v_pk_fma_f32 v[144:145], v[18:19], v[18:19], v[144:145]
	v_pk_fma_f32 v[142:143], v[30:31], v[30:31], v[142:143]
	v_pk_fma_f32 v[140:141], v[22:23], v[22:23], v[140:141]
	v_permlane32_swap_b32_e32 v132, v131
	v_pk_add_f32 v[140:141], v[140:141], v[142:143]
	v_pk_add_f32 v[142:143], v[144:145], v[146:147]
	v_pk_add_f32 v[144:145], v[148:149], v[154:155]
	v_pk_add_f32 v[146:147], v[156:157], v[158:159]
	v_pk_add_f32 v[140:141], v[142:143], v[140:141]
	v_pk_add_f32 v[144:145], v[146:147], v[144:145]
	v_pk_mul_f32 v[122:123], v[122:123], v[38:39]
	v_pk_mov_b32 v[142:143], v[140:141], v[144:145] op_sel:[1,0]
	v_mov_b32_e32 v141, v145
	v_pk_add_f32 v[140:141], v[142:143], v[140:141]
	v_pk_mul_f32 v[126:127], v[126:127], v[46:47]
	v_pk_add_f32 v[140:141], v[140:141], v[140:141] op_sel:[0,1] op_sel_hi:[1,0]
	v_pk_mul_f32 v[114:115], v[114:115], v[34:35]
	v_mov_b32_e32 v130, v140
	s_nop 1
	v_permlane32_swap_b32_e32 v140, v130
	v_mov_b32_e32 v141, v132
	v_pk_add_f32 v[130:131], v[140:141], v[130:131]
	v_pk_mul_f32 v[118:119], v[118:119], v[42:43]
	v_pk_fma_f32 v[130:131], v[130:131], s[0:1], v[152:153] op_sel_hi:[1,0,0]
	v_pk_mul_f32 v[124:125], v[124:125], v[40:41]
	v_mul_f32_e32 v132, 0x4b800000, v131
	v_cmp_gt_f32_e32 vcc, s1, v131
	v_pk_mul_f32 v[128:129], v[128:129], v[48:49]
	v_pk_mul_f32 v[116:117], v[116:117], v[36:37]
	v_pk_mul_f32 v[120:121], v[120:121], v[44:45]
	v_cndmask_b32_e32 v131, v131, v132, vcc
	v_mul_f32_e32 v132, 0x4b800000, v130
	v_cmp_gt_f32_e64 s[0:1], s1, v130
	v_pk_fma_f32 v[112:113], v[112:113], v[28:29], v[120:121]
	v_pk_fma_f32 v[104:105], v[104:105], v[20:21], v[116:117]
	v_pk_fma_f32 v[108:109], v[108:109], v[32:33], v[128:129]
	v_pk_fma_f32 v[100:101], v[100:101], v[24:25], v[124:125]
	v_pk_fma_f32 v[110:111], v[110:111], v[26:27], v[118:119]
	v_pk_fma_f32 v[102:103], v[102:103], v[18:19], v[114:115]
	v_pk_fma_f32 v[106:107], v[106:107], v[30:31], v[126:127]
	v_pk_fma_f32 v[98:99], v[98:99], v[22:23], v[122:123]
	v_rsq_f32_e32 v131, v131
	v_cndmask_b32_e64 v130, v130, v132, s[0:1]
	v_pk_add_f32 v[98:99], v[98:99], v[106:107]
	v_pk_add_f32 v[102:103], v[102:103], v[110:111]
	v_pk_add_f32 v[100:101], v[100:101], v[108:109]
	v_pk_add_f32 v[104:105], v[104:105], v[112:113]
	v_rsq_f32_e32 v132, v130
	v_pk_add_f32 v[100:101], v[104:105], v[100:101]
	v_pk_add_f32 v[98:99], v[102:103], v[98:99]
	v_mul_f32_e32 v130, 0x45800000, v131
	v_add_f32_e32 v98, v98, v99
	v_add_f32_e32 v99, v100, v101
	v_add_f32_e32 v98, v98, v99
	v_mov_b32_e32 v99, v98
	v_pk_mul_f32 v[90:91], v[90:91], v[38:39]
	v_pk_mul_f32 v[94:95], v[94:95], v[46:47]
	v_pk_mul_f32 v[82:83], v[82:83], v[34:35]
	v_pk_mul_f32 v[86:87], v[86:87], v[42:43]
	v_cndmask_b32_e32 v130, v131, v130, vcc
	v_mul_f32_e32 v131, 0x45800000, v132
	v_permlane32_swap_b32_e32 v98, v99
	v_pk_fma_f32 v[78:79], v[78:79], v[26:27], v[86:87]
	v_pk_fma_f32 v[70:71], v[70:71], v[18:19], v[82:83]
	v_pk_fma_f32 v[74:75], v[74:75], v[30:31], v[94:95]
	v_pk_fma_f32 v[66:67], v[66:67], v[22:23], v[90:91]
	v_cndmask_b32_e64 v131, v132, v131, s[0:1]
	v_add_f32_e32 v98, v98, v99
	v_pk_add_f32 v[66:67], v[66:67], v[74:75]
	v_pk_add_f32 v[70:71], v[70:71], v[78:79]
	v_mul_f32_e32 v139, v160, v130
	v_mul_f32_e32 v98, v98, v131
	v_pk_add_f32 v[66:67], v[70:71], v[66:67]
	v_cmp_gt_u32_e32 vcc, 32, v1
	v_add_f32_e32 v66, v66, v67
	v_pk_mul_f32 v[92:93], v[92:93], v[40:41]
	v_cndmask_b32_e32 v67, v98, v139, vcc
	v_add_f32_e32 v67, s12, v67
	v_pk_mul_f32 v[96:97], v[96:97], v[48:49]
	v_pk_mul_f32 v[84:85], v[84:85], v[36:37]
	v_pk_mul_f32 v[88:89], v[88:89], v[44:45]
	v_mul_f32_e32 v67, 0xbfb8aa3b, v67
	v_pk_fma_f32 v[80:81], v[80:81], v[28:29], v[88:89]
	v_pk_fma_f32 v[72:73], v[72:73], v[20:21], v[84:85]
	v_pk_fma_f32 v[76:77], v[76:77], v[32:33], v[96:97]
	v_pk_fma_f32 v[68:69], v[68:69], v[24:25], v[92:93]
	v_exp_f32_e32 v70, v67
	v_pk_add_f32 v[68:69], v[68:69], v[76:77]
	v_pk_add_f32 v[72:73], v[72:73], v[80:81]
	v_cmp_lt_i32_e64 s[0:1], 0, v151
	v_pk_add_f32 v[68:69], v[72:73], v[68:69]
	v_mov_b32_e32 v137, v136
	v_add_f32_e32 v67, v68, v69
	v_add_f32_e32 v67, v66, v67
	v_add_f32_e32 v66, 1.0, v70
	v_rcp_f32_e32 v66, v66
	v_mov_b32_e32 v69, 0xff800000
	v_mov_b32_e32 v138, v133
	v_mov_b32_e32 v68, v67
	v_cndmask_b32_e64 v70, v69, v66, s[0:1]
	v_mbcnt_lo_u32_b32 v66, -1, 0
	v_mbcnt_hi_u32_b32 v66, -1, v66
	v_permlane32_swap_b32_e32 v136, v137
	v_permlane32_swap_b32_e32 v133, v138
	v_permlane32_swap_b32_e32 v67, v68
	v_and_b32_e32 v86, 64, v66
	s_mov_b32 s14, 8
	s_mov_b32 s13, 0
	v_mov_b32_e32 v66, 0
	s_waitcnt lgkmcnt(0)
